# P6: next-unit gather offsets: four masked list loads issued together, one wait (were four serialized load+wait round trips per unit)
# baseline (speedup 1.0000x reference)
; template <class Epi, class Sched, bool ALIGN_EPI, bool FP8 = false>
; __device__ __forceinline__ void gemm_phase(PG8_LAS unsigned char* lds, const Gemm g, const Sched& S, const Epi& E, const int wid, const int lane) {
;     ...
;         if (GA && has_next) {
;             u32x4 q; q.x = S.tok_off(nxt, rA[0]) + cA2[0]; q.y = S.tok_off(nxt, rA[1]) + cA2[1]; q.z = S.tok_off(nxt, HALF + rA[0]) + cA2[0]; q.w = S.tok_off(nxt, HALF + rA[1]) + cA2[1];
;             *gslot = q;
;     __device__ __forceinline__ unsigned tok_off(const Unit& u, int r) const {
;         const int e = tileE[u.pm], local = (u.pm - tb[e]) * 256 + r;
;         int tok = local;
;         if (e < NE) tok = (local < cnt[e]) ? list[(size_t)e * LISTCAP + local] : 0;
;         return (unsigned)tok * K2;
;     }
.LBB0_731:
	s_lshl_b32 s6, s86, 2
	s_add_i32 s6, s6, 0x20800
	v_mov_b32_e32 v0, s6
	ds_read_b32 v1, v0
	s_waitcnt lgkmcnt(0)
	s_nop 0
	v_readfirstlane_b32 s38, v1
	s_nop 3
	s_lshl_b32 s6, s38, 2
	s_add_i32 s7, s6, 0x21000
	s_add_i32 s6, s6, 0x21200
	v_mov_b32_e32 v0, s7
	v_mov_b32_e32 v1, s6
	ds_read_b32 v0, v0
	ds_read_b32 v1, v1
	s_waitcnt lgkmcnt(0)
	v_sub_u32_e32 v0, s86, v0
	v_lshlrev_b32_e32 v4, 8, v0
	v_or_b32_e32 v6, 0x80, v4
	v_add_u32_e32 v0, v4, v199
	v_add_u32_e32 v2, v4, v204
	v_add_u32_e32 v4, v6, v199
	v_add_u32_e32 v6, v6, v204
	s_cmp_gt_i32 s38, 63
	s_cbranch_scc1 .LBB0_747
	s_ashr_i32 s39, s38, 31
	s_lshl_b64 s[40:41], s[38:39], 16
	s_add_u32 s40, s14, s40
	s_addc_u32 s41, s15, s41
	v_cmp_lt_i32_e32 vcc, v0, v1
	v_lshlrev_b32_e32 v220, 2, v0
	v_mov_b32_e32 v0, 0
	s_and_saveexec_b64 s[6:7], vcc
	s_cbranch_execz .Lp6a_g0
	global_load_dword v0, v220, s[40:41]
.Lp6a_g0:
	s_or_b64 exec, exec, s[6:7]
	v_cmp_lt_i32_e32 vcc, v2, v1
	v_lshlrev_b32_e32 v221, 2, v2
	v_mov_b32_e32 v2, 0
	s_and_saveexec_b64 s[6:7], vcc
	s_cbranch_execz .Lp6a_g1
	global_load_dword v2, v221, s[40:41]
.Lp6a_g1:
	s_or_b64 exec, exec, s[6:7]
	v_cmp_lt_i32_e32 vcc, v4, v1
	v_lshlrev_b32_e32 v222, 2, v4
	v_mov_b32_e32 v4, 0
	s_and_saveexec_b64 s[6:7], vcc
	s_cbranch_execz .Lp6a_g2
	global_load_dword v4, v222, s[40:41]
.Lp6a_g2:
	s_or_b64 exec, exec, s[6:7]
	v_cmp_lt_i32_e32 vcc, v6, v1
	v_lshlrev_b32_e32 v223, 2, v6
	v_mov_b32_e32 v6, 0
	s_and_saveexec_b64 s[6:7], vcc
	s_cbranch_execz .Lp6a_g3
	global_load_dword v6, v223, s[40:41]
.Lp6a_g3:
	s_or_b64 exec, exec, s[6:7]
	s_waitcnt vmcnt(0)
.LBB0_747:
	v_lshl_add_u32 v0, v0, 11, v198
	v_lshl_add_u32 v1, v2, 11, v196
	v_lshl_add_u32 v2, v4, 11, v198
	v_lshl_add_u32 v3, v6, 11, v196
	ds_write_b128 v201, v[0:3]
	s_andn2_b64 vcc, exec, s[26:27]
	v_mov_b32_e32 v195, 0
	s_cbranch_vccz .LBB0_726

; template <class Epi, class Sched, bool ALIGN_EPI, bool FP8 = false>
; __device__ __forceinline__ void gemm_phase(PG8_LAS unsigned char* lds, const Gemm g, const Sched& S, const Epi& E, const int wid, const int lane) {
;     ...
;         if (GA && has_next) {
;             u32x4 q; q.x = S.tok_off(nxt, rA[0]) + cA2[0]; q.y = S.tok_off(nxt, rA[1]) + cA2[1]; q.z = S.tok_off(nxt, HALF + rA[0]) + cA2[0]; q.w = S.tok_off(nxt, HALF + rA[1]) + cA2[1];
;             *gslot = q;
;     __device__ __forceinline__ unsigned tok_off(const Unit& u, int r) const {
;         const int e = tileE[u.pm], local = (u.pm - tb[e]) * 256 + r;
;         int tok = local;
;         if (e < NE) tok = (local < cnt[e]) ? list[(size_t)e * LISTCAP + local] : 0;
;         return (unsigned)tok * K2;
;     }
.LBB0_1641:
	s_lshl_b32 s6, s85, 2
	s_add_i32 s6, s6, 0x20800
	v_mov_b32_e32 v0, s6
	ds_read_b32 v1, v0
	s_waitcnt lgkmcnt(0)
	s_nop 0
	v_readfirstlane_b32 s38, v1
	s_nop 3
	s_lshl_b32 s6, s38, 2
	s_add_i32 s7, s6, 0x21000
	s_add_i32 s6, s6, 0x21200
	v_mov_b32_e32 v0, s7
	v_mov_b32_e32 v1, s6
	ds_read_b32 v0, v0
	ds_read_b32 v1, v1
	s_waitcnt lgkmcnt(0)
	v_sub_u32_e32 v0, s85, v0
	v_lshlrev_b32_e32 v4, 8, v0
	v_or_b32_e32 v6, 0x80, v4
	v_add_u32_e32 v0, v4, v199
	v_add_u32_e32 v2, v4, v204
	v_add_u32_e32 v4, v6, v199
	v_add_u32_e32 v6, v6, v204
	s_cmp_gt_i32 s38, 63
	s_cbranch_scc1 .LBB0_1657
	s_ashr_i32 s39, s38, 31
	s_lshl_b64 s[40:41], s[38:39], 16
	s_add_u32 s40, s14, s40
	s_addc_u32 s41, s15, s41
	v_cmp_lt_i32_e32 vcc, v0, v1
	v_lshlrev_b32_e32 v220, 2, v0
	v_mov_b32_e32 v0, 0
	s_and_saveexec_b64 s[6:7], vcc
	s_cbranch_execz .Lp6b_g0
	global_load_dword v0, v220, s[40:41]

; template <class Epi, class Sched, bool ALIGN_EPI, bool FP8 = false>
; __device__ __forceinline__ void gemm_phase(PG8_LAS unsigned char* lds, const Gemm g, const Sched& S, const Epi& E, const int wid, const int lane) {
;     ...
;             u32x4 q; q.x = S.tok_off(nxt, rA[0]) + cA2[0]; q.y = S.tok_off(nxt, rA[1]) + cA2[1]; q.z = S.tok_off(nxt, HALF + rA[0]) + cA2[0]; q.w = S.tok_off(nxt, HALF + rA[1]) + cA2[1];
;             *gslot = q;
.Lp6b_g3:
	s_or_b64 exec, exec, s[6:7]
	s_waitcnt vmcnt(0)
.LBB0_1657:
	v_lshl_add_u32 v0, v0, 11, v198
	v_lshl_add_u32 v1, v2, 11, v196
	v_lshl_add_u32 v2, v4, 11, v198
	v_lshl_add_u32 v3, v6, 11, v196
	ds_write_b128 v201, v[0:3]
	s_andn2_b64 vcc, exec, s[26:27]
	v_mov_b32_e32 v195, 0
	s_cbranch_vccz .LBB0_1636
